# P7: xor-8/4/2/1 butterfly steps (wave sums, top-4 arg-max) as DPP moves instead of ds_bpermute (bit-identical)
# speedup vs baseline: 1.0044x; 1.0044x over previous
.LBB0_682:
	v_lshl_add_u64 v[2:3], s[76:77], 0, v[28:29]
	v_add_co_u32_e32 v30, vcc, 0x54768000, v2
	s_add_i32 s22, s14, s15
	s_nop 0
	v_addc_co_u32_e32 v31, vcc, 0, v3, vcc
	global_load_dwordx2 v[226:227], v[30:31], off nt
	global_load_dwordx2 v[228:229], v[30:31], off offset:512 nt
	global_load_dwordx2 v[230:231], v[30:31], off offset:1024 nt
	global_load_dwordx2 v[232:233], v[30:31], off offset:1536 nt
	global_load_dwordx2 v[234:235], v[30:31], off offset:2048 nt
	global_load_dwordx2 v[236:237], v[30:31], off offset:2560 nt
	global_load_dwordx2 v[238:239], v[30:31], off offset:3072 nt
	global_load_dwordx2 v[240:241], v[30:31], off offset:3584 nt
	s_add_i32 s98, s22, 1
	s_ashr_i32 s99, s98, 31
	s_lshl_b64 s[98:99], s[98:99], 12
	v_lshl_add_u64 v[252:253], v[22:23], 0, s[98:99]
	global_load_dwordx2 v[242:243], v[252:253], off nt
	global_load_dwordx2 v[244:245], v[252:253], off offset:512 nt
	global_load_dwordx2 v[246:247], v[252:253], off offset:1024 nt
	global_load_dwordx2 v[248:249], v[252:253], off offset:1536 nt
	global_load_dwordx2 v[250:251], v[252:253], off offset:2048 nt
	s_ashr_i32 s0, s22, 13
	s_mulk_i32 s0, 0x3000
	s_ashr_i32 s1, s0, 31
	s_lshl_b64 s[0:1], s[0:1], 2
	s_add_u32 s20, s3, s0
	s_addc_u32 s21, s24, s1
	s_add_u32 s0, s20, 0x6000
	s_addc_u32 s1, s21, 0
	s_add_u32 s20, s20, 0x8000
	s_addc_u32 s21, s21, 0
	s_waitcnt vmcnt(12)
	v_and_b32_e32 v3, 0xffff0000, v226
	s_waitcnt vmcnt(11)
	v_and_b32_e32 v57, 0xffff0000, v228
	v_lshlrev_b32_e32 v2, 16, v226
	v_mul_f32_e32 v34, v3, v3
	v_lshlrev_b32_e32 v56, 16, v228
	v_mul_f32_e32 v32, v57, v57
	v_lshlrev_b32_e32 v4, 16, v227
	v_fmac_f32_e32 v34, v2, v2
	v_lshlrev_b32_e32 v58, 16, v229
	v_fmac_f32_e32 v32, v56, v56
	v_and_b32_e32 v5, 0xffff0000, v227
	v_fmac_f32_e32 v34, v4, v4
	v_and_b32_e32 v59, 0xffff0000, v229
	v_fmac_f32_e32 v32, v58, v58
	v_fmac_f32_e32 v34, v5, v5
	v_fmac_f32_e32 v32, v59, v59
	v_add_f32_e32 v34, v34, v32
	s_waitcnt vmcnt(10)
	v_and_b32_e32 v53, 0xffff0000, v230
	v_lshlrev_b32_e32 v52, 16, v230
	v_mul_f32_e32 v32, v53, v53
	v_lshlrev_b32_e32 v54, 16, v231
	v_fmac_f32_e32 v32, v52, v52
	v_and_b32_e32 v55, 0xffff0000, v231
	v_fmac_f32_e32 v32, v54, v54
	v_fmac_f32_e32 v32, v55, v55
	v_add_f32_e32 v34, v34, v32
	s_waitcnt vmcnt(9)
	v_and_b32_e32 v49, 0xffff0000, v232
	v_lshlrev_b32_e32 v48, 16, v232
	v_mul_f32_e32 v32, v49, v49
	v_lshlrev_b32_e32 v50, 16, v233
	v_fmac_f32_e32 v32, v48, v48
	v_and_b32_e32 v51, 0xffff0000, v233
	v_fmac_f32_e32 v32, v50, v50
	v_fmac_f32_e32 v32, v51, v51
	v_add_f32_e32 v36, v34, v32
	s_waitcnt vmcnt(8)
	v_and_b32_e32 v42, 0xffff0000, v234
	s_waitcnt vmcnt(7)
	v_and_b32_e32 v43, 0xffff0000, v236
	v_lshlrev_b32_e32 v41, 16, v236
	v_lshlrev_b32_e32 v40, 16, v234
	v_lshlrev_b32_e32 v44, 16, v235
	v_and_b32_e32 v46, 0xffff0000, v235
	v_pk_mul_f32 v[32:33], v[42:43], v[42:43]
	v_lshlrev_b32_e32 v45, 16, v237
	v_pk_fma_f32 v[32:33], v[40:41], v[40:41], v[32:33]
	v_and_b32_e32 v47, 0xffff0000, v237
	v_pk_fma_f32 v[32:33], v[44:45], v[44:45], v[32:33]
	s_nop 0
	v_pk_fma_f32 v[32:33], v[46:47], v[46:47], v[32:33]
	s_nop 0
	v_add_f32_e32 v32, v36, v32
	global_load_dwordx4 v[214:217], v202, s[0:1]
	global_load_dwordx4 v[218:221], v202, s[20:21]
	global_load_dwordx4 v[222:225], v[8:9], off
	v_add_f32_e32 v38, v32, v33
	s_waitcnt vmcnt(9)
	v_and_b32_e32 v32, 0xffff0000, v238
	s_waitcnt vmcnt(8)
	v_and_b32_e32 v33, 0xffff0000, v240
	v_lshlrev_b32_e32 v31, 16, v240
	v_lshlrev_b32_e32 v30, 16, v238
	v_lshlrev_b32_e32 v34, 16, v239
	v_and_b32_e32 v36, 0xffff0000, v239
	v_pk_mul_f32 v[60:61], v[32:33], v[32:33]
	v_lshlrev_b32_e32 v35, 16, v241
	v_pk_fma_f32 v[60:61], v[30:31], v[30:31], v[60:61]
	v_and_b32_e32 v37, 0xffff0000, v241
	v_pk_fma_f32 v[60:61], v[34:35], v[34:35], v[60:61]
	global_load_dwordx2 v[226:227], v[252:253], off offset:2560 nt
	global_load_dwordx2 v[228:229], v[252:253], off offset:3072 nt
	global_load_dwordx2 v[230:231], v[252:253], off offset:3584 nt
	s_waitcnt vmcnt(4)
	v_pk_add_f32 v[218:219], v[218:219], 1.0 op_sel_hi:[1,0]
	v_pk_fma_f32 v[60:61], v[36:37], v[36:37], v[60:61]
	s_nop 0
	v_add_f32_e32 v38, v38, v60
	v_add_f32_e32 v38, v38, v61
	ds_bpermute_b32 v60, v189, v38
	s_waitcnt lgkmcnt(0)
	v_add_f32_e32 v38, v38, v60
	ds_bpermute_b32 v60, v192, v38
	s_waitcnt lgkmcnt(0)
	v_add_f32_e32 v38, v38, v60
	s_nop 1
	v_mov_b32_dpp v60, v38 row_ror:8 row_mask:0xf bank_mask:0xf
	s_waitcnt lgkmcnt(0)
	v_add_f32_e32 v38, v38, v60
	s_nop 1
	v_mov_b32_dpp v60, v38 row_ror:4 row_mask:0xf bank_mask:0xf
	s_waitcnt lgkmcnt(0)
	v_add_f32_e32 v38, v38, v60
	s_nop 1
	v_mov_b32_dpp v60, v38 quad_perm:[2,3,0,1] row_mask:0xf bank_mask:0xf
	s_waitcnt lgkmcnt(0)
	v_add_f32_e32 v38, v38, v60
	s_nop 1
	v_mov_b32_dpp v60, v38 quad_perm:[1,0,3,2] row_mask:0xf bank_mask:0xf
	s_waitcnt lgkmcnt(0)
	v_add_f32_e32 v38, v38, v60
	v_fmamk_f32 v38, v38, 0x3a000000, v201
	v_cmp_gt_f32_e32 vcc, s27, v38
	v_mul_f32_e32 v60, 0x4b800000, v38
	s_nop 0
	v_cndmask_b32_e32 v38, v38, v60, vcc
	v_rsq_f32_e32 v38, v38
	s_nop 0
	v_mul_f32_e32 v60, 0x45800000, v38
	v_cndmask_b32_e32 v38, v38, v60, vcc
	v_pk_mul_f32 v[2:3], v[2:3], v[38:39] op_sel_hi:[1,0]
	v_pk_mul_f32 v[4:5], v[4:5], v[38:39] op_sel_hi:[1,0]
	s_waitcnt vmcnt(3)
	v_pk_mul_f32 v[2:3], v[222:223], v[2:3]
	v_pk_mul_f32 v[4:5], v[224:225], v[4:5]
	v_pk_fma_f32 v[2:3], v[218:219], v[2:3], v[214:215]
	v_mov_b32_e32 v214, 0
	v_cvt_pk_fp8_f32 v214, v2, v3
	v_pk_add_f32 v[60:61], v[220:221], 1.0 op_sel_hi:[1,0]
	v_pk_mul_f32 v[56:57], v[56:57], v[38:39] op_sel_hi:[1,0]
	v_pk_fma_f32 v[4:5], v[60:61], v[4:5], v[216:217]
	v_lshl_add_u64 v[60:61], s[76:77], 0, v[26:27]
	v_cvt_pk_fp8_f32 v214, v4, v5 op_sel:[0,0,1]
	v_add_co_u32_e32 v60, vcc, s28, v60
	ds_write_b128 v199, v[2:5]
	s_nop 0
	v_addc_co_u32_e32 v61, vcc, 0, v61, vcc
	s_nop 1
	v_mov_b32_e32 v240, v214
	global_load_dwordx4 v[2:5], v203, s[0:1]
	s_nop 0
	global_load_dwordx4 v[214:217], v203, s[20:21]
	global_load_dwordx4 v[218:221], v[8:9], off offset:1024
	global_store_dword v[60:61], v240, off
	v_pk_mul_f32 v[58:59], v[58:59], v[38:39] op_sel_hi:[1,0]
	v_pk_mul_f32 v[52:53], v[52:53], v[38:39] op_sel_hi:[1,0]
	v_pk_mul_f32 v[54:55], v[54:55], v[38:39] op_sel_hi:[1,0]
	v_pk_mul_f32 v[48:49], v[48:49], v[38:39] op_sel_hi:[1,0]
	v_pk_mul_f32 v[50:51], v[50:51], v[38:39] op_sel_hi:[1,0]
	s_waitcnt vmcnt(2)
	v_pk_add_f32 v[214:215], v[214:215], 1.0 op_sel_hi:[1,0]
	s_waitcnt vmcnt(1)
	v_pk_mul_f32 v[56:57], v[218:219], v[56:57]
	v_pk_mul_f32 v[58:59], v[220:221], v[58:59]
	v_pk_fma_f32 v[2:3], v[214:215], v[56:57], v[2:3]
	v_mov_b32_e32 v56, 0
	v_cvt_pk_fp8_f32 v56, v2, v3
	v_pk_add_f32 v[216:217], v[216:217], 1.0 op_sel_hi:[1,0]
	s_nop 0
	v_pk_fma_f32 v[4:5], v[216:217], v[58:59], v[4:5]
	ds_write_b128 v199, v[2:5] offset:1024
	v_cvt_pk_fp8_f32 v56, v4, v5 op_sel:[0,0,1]
	s_nop 1
	v_mov_b32_e32 v240, v56
	global_load_dwordx4 v[2:5], v204, s[0:1]
	s_nop 0
	global_load_dwordx4 v[56:59], v204, s[20:21]
	global_load_dwordx4 v[214:217], v[8:9], off offset:2048
	global_store_dword v[60:61], v240, off offset:256
	s_waitcnt vmcnt(2)
	v_pk_add_f32 v[56:57], v[56:57], 1.0 op_sel_hi:[1,0]
	s_waitcnt vmcnt(1)
	v_pk_mul_f32 v[52:53], v[214:215], v[52:53]
	v_pk_mul_f32 v[54:55], v[216:217], v[54:55]
	v_pk_fma_f32 v[2:3], v[56:57], v[52:53], v[2:3]
	v_mov_b32_e32 v52, 0
	v_cvt_pk_fp8_f32 v52, v2, v3
	v_pk_add_f32 v[58:59], v[58:59], 1.0 op_sel_hi:[1,0]
	s_nop 0
	v_pk_fma_f32 v[4:5], v[58:59], v[54:55], v[4:5]
	ds_write_b128 v199, v[2:5] offset:2048
	v_cvt_pk_fp8_f32 v52, v4, v5 op_sel:[0,0,1]
	s_nop 1
	v_mov_b32_e32 v240, v52
	global_load_dwordx4 v[2:5], v205, s[0:1]
	s_nop 0
	global_load_dwordx4 v[52:55], v205, s[20:21]
	global_load_dwordx4 v[56:59], v[8:9], off offset:3072
	global_store_dword v[60:61], v240, off offset:512
	s_waitcnt vmcnt(2)
	v_pk_add_f32 v[52:53], v[52:53], 1.0 op_sel_hi:[1,0]
	s_waitcnt vmcnt(1)
	v_pk_mul_f32 v[48:49], v[48:49], v[56:57]
	v_pk_mul_f32 v[50:51], v[50:51], v[58:59]
	v_pk_fma_f32 v[2:3], v[52:53], v[48:49], v[2:3]
	v_mov_b32_e32 v48, 0
	v_cvt_pk_fp8_f32 v48, v2, v3
	v_pk_add_f32 v[54:55], v[54:55], 1.0 op_sel_hi:[1,0]
	v_mov_b32_e32 v58, v40
	v_pk_fma_f32 v[4:5], v[54:55], v[50:51], v[4:5]
	ds_write_b128 v199, v[2:5] offset:3072
	v_cvt_pk_fp8_f32 v48, v4, v5 op_sel:[0,0,1]
	v_mov_b32_e32 v59, v42
	v_pk_mul_f32 v[58:59], v[58:59], v[38:39] op_sel_hi:[1,0]
	v_mov_b32_e32 v40, 0
	s_nop 1
	v_mov_b32_e32 v240, v48
	global_load_dwordx4 v[2:5], v206, s[0:1]
	s_nop 0
	global_load_dwordx4 v[48:51], v206, s[20:21]
	global_load_dwordx4 v[52:55], v[10:11], off
	global_store_dword v[60:61], v240, off offset:768
	v_mov_b32_e32 v56, v44
	v_mov_b32_e32 v57, v46
	v_pk_mul_f32 v[56:57], v[56:57], v[38:39] op_sel_hi:[1,0]
	v_mov_b32_e32 v42, v41
	v_mov_b32_e32 v46, v45
	v_pk_mul_f32 v[44:45], v[46:47], v[38:39] op_sel_hi:[1,0]
	s_waitcnt vmcnt(2)
	v_pk_add_f32 v[48:49], v[48:49], 1.0 op_sel_hi:[1,0]
	s_waitcnt vmcnt(1)
	v_pk_mul_f32 v[52:53], v[58:59], v[52:53]
	v_pk_mul_f32 v[54:55], v[56:57], v[54:55]
	v_pk_fma_f32 v[2:3], v[48:49], v[52:53], v[2:3]
	v_pk_add_f32 v[50:51], v[50:51], 1.0 op_sel_hi:[1,0]
	v_cvt_pk_fp8_f32 v40, v2, v3
	v_pk_fma_f32 v[4:5], v[50:51], v[54:55], v[4:5]
	ds_write_b128 v199, v[2:5] offset:4096
	v_cvt_pk_fp8_f32 v40, v4, v5 op_sel:[0,0,1]
	s_nop 1
	v_mov_b32_e32 v240, v40
	global_load_dwordx4 v[2:5], v207, s[0:1]
	global_load_dwordx4 v[48:51], v207, s[20:21]
	global_load_dwordx4 v[52:55], v[12:13], off
	global_store_dword v[60:61], v240, off offset:1024
	v_pk_mul_f32 v[40:41], v[42:43], v[38:39] op_sel_hi:[1,0]
	s_waitcnt vmcnt(2)
	v_pk_add_f32 v[46:47], v[48:49], 1.0 op_sel_hi:[1,0]
	s_waitcnt vmcnt(1)
	v_pk_mul_f32 v[40:41], v[40:41], v[52:53]
	v_pk_mul_f32 v[42:43], v[44:45], v[54:55]
	v_pk_fma_f32 v[2:3], v[46:47], v[40:41], v[2:3]
	v_mov_b32_e32 v40, 0
	v_cvt_pk_fp8_f32 v40, v2, v3
	v_pk_add_f32 v[44:45], v[50:51], 1.0 op_sel_hi:[1,0]
	v_mov_b32_e32 v50, v30
	v_pk_fma_f32 v[4:5], v[44:45], v[42:43], v[4:5]
	ds_write_b128 v199, v[2:5] offset:5120
	v_cvt_pk_fp8_f32 v40, v4, v5 op_sel:[0,0,1]
	v_mov_b32_e32 v51, v32
	v_pk_mul_f32 v[50:51], v[50:51], v[38:39] op_sel_hi:[1,0]
	v_mov_b32_e32 v30, 0
	s_nop 1
	v_mov_b32_e32 v240, v40
	global_load_dwordx4 v[2:5], v208, s[0:1]
	s_nop 0
	global_load_dwordx4 v[40:43], v208, s[20:21]
	global_load_dwordx4 v[44:47], v[14:15], off
	global_store_dword v[60:61], v240, off offset:1280
	v_mov_b32_e32 v48, v34
	v_mov_b32_e32 v49, v36
	v_pk_mul_f32 v[48:49], v[48:49], v[38:39] op_sel_hi:[1,0]
	v_mov_b32_e32 v32, v31
	v_mov_b32_e32 v36, v35
	v_pk_mul_f32 v[34:35], v[36:37], v[38:39] op_sel_hi:[1,0]
	s_waitcnt vmcnt(2)
	v_pk_add_f32 v[40:41], v[40:41], 1.0 op_sel_hi:[1,0]
	s_waitcnt vmcnt(1)
	v_pk_mul_f32 v[44:45], v[50:51], v[44:45]
	v_pk_mul_f32 v[46:47], v[48:49], v[46:47]
	v_pk_fma_f32 v[2:3], v[40:41], v[44:45], v[2:3]
	v_pk_add_f32 v[42:43], v[42:43], 1.0 op_sel_hi:[1,0]
	v_cvt_pk_fp8_f32 v30, v2, v3
	v_pk_fma_f32 v[4:5], v[42:43], v[46:47], v[4:5]
	ds_write_b128 v199, v[2:5] offset:6144
	v_cvt_pk_fp8_f32 v30, v4, v5 op_sel:[0,0,1]
	s_nop 1
	v_mov_b32_e32 v240, v30
	global_load_dwordx4 v[2:5], v209, s[0:1]
	global_load_dwordx4 v[40:43], v209, s[20:21]
	global_load_dwordx4 v[44:47], v[16:17], off
	global_store_dword v[60:61], v240, off offset:1536
	v_pk_mul_f32 v[30:31], v[32:33], v[38:39] op_sel_hi:[1,0]
	s_add_i32 s0, s22, 1
	s_ashr_i32 s1, s0, 31
	s_lshl_b64 s[20:21], s[0:1], 12
	s_lshl_b64 s[22:23], s[0:1], 11
	s_ashr_i32 s0, s0, 13
	s_mulk_i32 s0, 0x3000
	s_ashr_i32 s1, s0, 31
	s_lshl_b64 s[0:1], s[0:1], 2
	s_waitcnt vmcnt(2)
	v_pk_add_f32 v[36:37], v[40:41], 1.0 op_sel_hi:[1,0]
	s_waitcnt vmcnt(1)
	v_pk_mul_f32 v[30:31], v[30:31], v[44:45]
	v_pk_mul_f32 v[32:33], v[34:35], v[46:47]
	v_pk_fma_f32 v[2:3], v[36:37], v[30:31], v[2:3]
	v_mov_b32_e32 v30, 0
	v_cvt_pk_fp8_f32 v30, v2, v3
	v_pk_add_f32 v[34:35], v[42:43], 1.0 op_sel_hi:[1,0]
	s_nop 0
	v_pk_fma_f32 v[4:5], v[34:35], v[32:33], v[4:5]
	ds_write_b128 v199, v[2:5] offset:7168
	v_cvt_pk_fp8_f32 v30, v4, v5 op_sel:[0,0,1]
	global_store_dword v[60:61], v30, off offset:1792
	v_lshl_add_u64 v[30:31], v[22:23], 0, s[20:21]
	s_add_u32 s20, s3, s0
	s_addc_u32 s21, s24, s1
	s_add_u32 s0, s20, 0x6000
	s_addc_u32 s1, s21, 0
	s_add_u32 s20, s20, 0x8000
	s_addc_u32 s21, s21, 0
	v_and_b32_e32 v3, 0xffff0000, v242
	v_and_b32_e32 v57, 0xffff0000, v244
	v_lshlrev_b32_e32 v2, 16, v242
	v_mul_f32_e32 v34, v3, v3
	v_lshlrev_b32_e32 v56, 16, v244
	v_mul_f32_e32 v32, v57, v57
	v_lshlrev_b32_e32 v4, 16, v243
	v_fmac_f32_e32 v34, v2, v2
	v_lshlrev_b32_e32 v58, 16, v245
	v_fmac_f32_e32 v32, v56, v56
	v_and_b32_e32 v5, 0xffff0000, v243
	v_fmac_f32_e32 v34, v4, v4
	v_and_b32_e32 v59, 0xffff0000, v245
	v_fmac_f32_e32 v32, v58, v58
	v_fmac_f32_e32 v34, v5, v5
	v_fmac_f32_e32 v32, v59, v59
	v_add_f32_e32 v34, v34, v32
	v_and_b32_e32 v53, 0xffff0000, v246
	v_lshlrev_b32_e32 v52, 16, v246
	v_mul_f32_e32 v32, v53, v53
	v_lshlrev_b32_e32 v54, 16, v247
	v_fmac_f32_e32 v32, v52, v52
	v_and_b32_e32 v55, 0xffff0000, v247
	v_fmac_f32_e32 v32, v54, v54
	v_fmac_f32_e32 v32, v55, v55
	v_add_f32_e32 v34, v34, v32
	v_and_b32_e32 v49, 0xffff0000, v248
	v_lshlrev_b32_e32 v48, 16, v248
	v_mul_f32_e32 v32, v49, v49
	v_lshlrev_b32_e32 v50, 16, v249
	v_fmac_f32_e32 v32, v48, v48
	v_and_b32_e32 v51, 0xffff0000, v249
	v_fmac_f32_e32 v32, v50, v50
	v_fmac_f32_e32 v32, v51, v51
	v_add_f32_e32 v36, v34, v32
	v_and_b32_e32 v42, 0xffff0000, v250
	v_and_b32_e32 v43, 0xffff0000, v226
	v_lshlrev_b32_e32 v41, 16, v226
	v_lshlrev_b32_e32 v40, 16, v250
	v_lshlrev_b32_e32 v44, 16, v251
	v_and_b32_e32 v46, 0xffff0000, v251
	v_pk_mul_f32 v[32:33], v[42:43], v[42:43]
	v_lshlrev_b32_e32 v45, 16, v227
	v_pk_fma_f32 v[32:33], v[40:41], v[40:41], v[32:33]
	v_and_b32_e32 v47, 0xffff0000, v227
	v_pk_fma_f32 v[32:33], v[44:45], v[44:45], v[32:33]
	s_nop 0
	v_pk_fma_f32 v[32:33], v[46:47], v[46:47], v[32:33]
	s_nop 0
	v_add_f32_e32 v32, v36, v32
	global_load_dwordx4 v[214:217], v202, s[0:1]
	global_load_dwordx4 v[218:221], v202, s[20:21]
	global_load_dwordx4 v[222:225], v[8:9], off
	v_add_f32_e32 v38, v32, v33
	s_waitcnt vmcnt(4)
	v_and_b32_e32 v32, 0xffff0000, v228
	s_waitcnt vmcnt(3)
	v_and_b32_e32 v33, 0xffff0000, v230
	v_lshlrev_b32_e32 v31, 16, v230
	v_lshlrev_b32_e32 v30, 16, v228
	v_lshlrev_b32_e32 v34, 16, v229
	v_and_b32_e32 v36, 0xffff0000, v229
	v_pk_mul_f32 v[60:61], v[32:33], v[32:33]
	v_lshlrev_b32_e32 v35, 16, v231
	v_pk_fma_f32 v[60:61], v[30:31], v[30:31], v[60:61]
	v_and_b32_e32 v37, 0xffff0000, v231
	v_pk_fma_f32 v[60:61], v[34:35], v[34:35], v[60:61]
	s_waitcnt vmcnt(1)
	v_pk_add_f32 v[218:219], v[218:219], 1.0 op_sel_hi:[1,0]
	v_pk_fma_f32 v[60:61], v[36:37], v[36:37], v[60:61]
	s_nop 0
	v_add_f32_e32 v38, v38, v60
	v_add_f32_e32 v38, v38, v61
	ds_bpermute_b32 v60, v189, v38
	s_waitcnt lgkmcnt(0)
	v_add_f32_e32 v38, v38, v60
	ds_bpermute_b32 v60, v192, v38
	s_waitcnt lgkmcnt(0)
	v_add_f32_e32 v38, v38, v60
	s_nop 1
	v_mov_b32_dpp v60, v38 row_ror:8 row_mask:0xf bank_mask:0xf
	s_waitcnt lgkmcnt(0)
	v_add_f32_e32 v38, v38, v60
	s_nop 1
	v_mov_b32_dpp v60, v38 row_ror:4 row_mask:0xf bank_mask:0xf
	s_waitcnt lgkmcnt(0)
	v_add_f32_e32 v38, v38, v60
	s_nop 1
	v_mov_b32_dpp v60, v38 quad_perm:[2,3,0,1] row_mask:0xf bank_mask:0xf
	s_waitcnt lgkmcnt(0)
	v_add_f32_e32 v38, v38, v60
	s_nop 1
	v_mov_b32_dpp v60, v38 quad_perm:[1,0,3,2] row_mask:0xf bank_mask:0xf
	s_waitcnt lgkmcnt(0)
	v_add_f32_e32 v38, v38, v60
	v_fmamk_f32 v38, v38, 0x3a000000, v201
	v_cmp_gt_f32_e32 vcc, s27, v38
	v_mul_f32_e32 v60, 0x4b800000, v38
	s_nop 0
	v_cndmask_b32_e32 v38, v38, v60, vcc
	v_rsq_f32_e32 v38, v38
	s_nop 0
	v_mul_f32_e32 v60, 0x45800000, v38
	v_cndmask_b32_e32 v38, v38, v60, vcc
	v_pk_mul_f32 v[2:3], v[2:3], v[38:39] op_sel_hi:[1,0]
	v_pk_mul_f32 v[4:5], v[4:5], v[38:39] op_sel_hi:[1,0]
	s_waitcnt vmcnt(0)
	v_pk_mul_f32 v[2:3], v[222:223], v[2:3]
	v_pk_mul_f32 v[4:5], v[224:225], v[4:5]
	v_pk_fma_f32 v[2:3], v[218:219], v[2:3], v[214:215]
	v_mov_b32_e32 v214, 0
	v_cvt_pk_fp8_f32 v214, v2, v3
	v_pk_add_f32 v[60:61], v[220:221], 1.0 op_sel_hi:[1,0]
	v_pk_mul_f32 v[56:57], v[56:57], v[38:39] op_sel_hi:[1,0]
	v_pk_fma_f32 v[4:5], v[60:61], v[4:5], v[216:217]
	v_lshl_add_u64 v[60:61], v[24:25], 0, s[22:23]
	v_cvt_pk_fp8_f32 v214, v4, v5 op_sel:[0,0,1]
	ds_write_b128 v200, v[2:5]
	v_pk_mul_f32 v[58:59], v[58:59], v[38:39] op_sel_hi:[1,0]
	v_pk_mul_f32 v[52:53], v[52:53], v[38:39] op_sel_hi:[1,0]
	s_nop 1
	v_mov_b32_e32 v240, v214
	global_load_dwordx4 v[2:5], v203, s[0:1]
	s_nop 0
	global_load_dwordx4 v[214:217], v203, s[20:21]
	global_load_dwordx4 v[218:221], v[8:9], off offset:1024
	global_store_dword v[60:61], v240, off
	v_pk_mul_f32 v[54:55], v[54:55], v[38:39] op_sel_hi:[1,0]
	v_pk_mul_f32 v[48:49], v[48:49], v[38:39] op_sel_hi:[1,0]
	v_pk_mul_f32 v[50:51], v[50:51], v[38:39] op_sel_hi:[1,0]
	s_waitcnt vmcnt(2)
	v_pk_add_f32 v[214:215], v[214:215], 1.0 op_sel_hi:[1,0]
	s_waitcnt vmcnt(1)
	v_pk_mul_f32 v[56:57], v[218:219], v[56:57]
	v_pk_mul_f32 v[58:59], v[220:221], v[58:59]
	v_pk_fma_f32 v[2:3], v[214:215], v[56:57], v[2:3]
	v_mov_b32_e32 v56, 0
	v_cvt_pk_fp8_f32 v56, v2, v3
	v_pk_add_f32 v[216:217], v[216:217], 1.0 op_sel_hi:[1,0]
	s_nop 0
	v_pk_fma_f32 v[4:5], v[216:217], v[58:59], v[4:5]
	ds_write_b128 v200, v[2:5] offset:1024
	v_cvt_pk_fp8_f32 v56, v4, v5 op_sel:[0,0,1]
	s_nop 1
	v_mov_b32_e32 v240, v56
	global_load_dwordx4 v[2:5], v204, s[0:1]
	s_nop 0
	global_load_dwordx4 v[56:59], v204, s[20:21]
	global_load_dwordx4 v[214:217], v[8:9], off offset:2048
	global_store_dword v[60:61], v240, off offset:256
	s_waitcnt vmcnt(2)
	v_pk_add_f32 v[56:57], v[56:57], 1.0 op_sel_hi:[1,0]
	s_waitcnt vmcnt(1)
	v_pk_mul_f32 v[52:53], v[214:215], v[52:53]
	v_pk_mul_f32 v[54:55], v[216:217], v[54:55]
	v_pk_fma_f32 v[2:3], v[56:57], v[52:53], v[2:3]
	v_mov_b32_e32 v52, 0
	v_cvt_pk_fp8_f32 v52, v2, v3
	v_pk_add_f32 v[58:59], v[58:59], 1.0 op_sel_hi:[1,0]
	s_nop 0
	v_pk_fma_f32 v[4:5], v[58:59], v[54:55], v[4:5]
	ds_write_b128 v200, v[2:5] offset:2048
	v_cvt_pk_fp8_f32 v52, v4, v5 op_sel:[0,0,1]
	s_nop 1
	v_mov_b32_e32 v240, v52
	global_load_dwordx4 v[2:5], v205, s[0:1]
	s_nop 0
	global_load_dwordx4 v[52:55], v205, s[20:21]
	global_load_dwordx4 v[56:59], v[8:9], off offset:3072
	global_store_dword v[60:61], v240, off offset:512
	s_waitcnt vmcnt(2)
	v_pk_add_f32 v[52:53], v[52:53], 1.0 op_sel_hi:[1,0]
	s_waitcnt vmcnt(1)
	v_pk_mul_f32 v[48:49], v[48:49], v[56:57]
	v_pk_mul_f32 v[50:51], v[50:51], v[58:59]
	v_pk_fma_f32 v[2:3], v[52:53], v[48:49], v[2:3]
	v_mov_b32_e32 v48, 0
	v_cvt_pk_fp8_f32 v48, v2, v3
	v_pk_add_f32 v[54:55], v[54:55], 1.0 op_sel_hi:[1,0]
	v_mov_b32_e32 v58, v40
	v_pk_fma_f32 v[4:5], v[54:55], v[50:51], v[4:5]
	ds_write_b128 v200, v[2:5] offset:3072
	v_cvt_pk_fp8_f32 v48, v4, v5 op_sel:[0,0,1]
	v_mov_b32_e32 v59, v42
	v_pk_mul_f32 v[58:59], v[58:59], v[38:39] op_sel_hi:[1,0]
	v_mov_b32_e32 v40, 0
	s_nop 1
	v_mov_b32_e32 v240, v48
	global_load_dwordx4 v[2:5], v206, s[0:1]
	s_nop 0
	global_load_dwordx4 v[48:51], v206, s[20:21]
	global_load_dwordx4 v[52:55], v[10:11], off
	global_store_dword v[60:61], v240, off offset:768
	v_mov_b32_e32 v56, v44
	v_mov_b32_e32 v57, v46
	v_pk_mul_f32 v[56:57], v[56:57], v[38:39] op_sel_hi:[1,0]
	v_mov_b32_e32 v42, v41
	v_mov_b32_e32 v46, v45
	v_pk_mul_f32 v[44:45], v[46:47], v[38:39] op_sel_hi:[1,0]
	s_waitcnt vmcnt(2)
	v_pk_add_f32 v[48:49], v[48:49], 1.0 op_sel_hi:[1,0]
	s_waitcnt vmcnt(1)
	v_pk_mul_f32 v[52:53], v[58:59], v[52:53]
	v_pk_mul_f32 v[54:55], v[56:57], v[54:55]
	v_pk_fma_f32 v[2:3], v[48:49], v[52:53], v[2:3]
	v_pk_add_f32 v[50:51], v[50:51], 1.0 op_sel_hi:[1,0]
	v_cvt_pk_fp8_f32 v40, v2, v3
	v_pk_fma_f32 v[4:5], v[50:51], v[54:55], v[4:5]
	ds_write_b128 v200, v[2:5] offset:4096
	v_cvt_pk_fp8_f32 v40, v4, v5 op_sel:[0,0,1]
	s_nop 1
	v_mov_b32_e32 v240, v40
	global_load_dwordx4 v[2:5], v207, s[0:1]
	global_load_dwordx4 v[48:51], v207, s[20:21]
	global_load_dwordx4 v[52:55], v[12:13], off
	global_store_dword v[60:61], v240, off offset:1024
	v_pk_mul_f32 v[40:41], v[42:43], v[38:39] op_sel_hi:[1,0]
	s_waitcnt vmcnt(2)
	v_pk_add_f32 v[46:47], v[48:49], 1.0 op_sel_hi:[1,0]
	s_waitcnt vmcnt(1)
	v_pk_mul_f32 v[40:41], v[40:41], v[52:53]
	v_pk_mul_f32 v[42:43], v[44:45], v[54:55]
	v_pk_fma_f32 v[2:3], v[46:47], v[40:41], v[2:3]
	v_mov_b32_e32 v40, 0
	v_cvt_pk_fp8_f32 v40, v2, v3
	v_pk_add_f32 v[44:45], v[50:51], 1.0 op_sel_hi:[1,0]
	v_mov_b32_e32 v50, v30
	v_pk_fma_f32 v[4:5], v[44:45], v[42:43], v[4:5]
	ds_write_b128 v200, v[2:5] offset:5120
	v_cvt_pk_fp8_f32 v40, v4, v5 op_sel:[0,0,1]
	v_mov_b32_e32 v51, v32
	v_pk_mul_f32 v[50:51], v[50:51], v[38:39] op_sel_hi:[1,0]
	v_mov_b32_e32 v30, 0
	s_nop 1
	v_mov_b32_e32 v240, v40
	global_load_dwordx4 v[2:5], v208, s[0:1]
	s_nop 0
	global_load_dwordx4 v[40:43], v208, s[20:21]
	global_load_dwordx4 v[44:47], v[14:15], off
	global_store_dword v[60:61], v240, off offset:1280
	v_mov_b32_e32 v48, v34
	v_mov_b32_e32 v49, v36
	v_pk_mul_f32 v[48:49], v[48:49], v[38:39] op_sel_hi:[1,0]
	v_mov_b32_e32 v32, v31
	v_mov_b32_e32 v36, v35
	v_pk_mul_f32 v[34:35], v[36:37], v[38:39] op_sel_hi:[1,0]
	s_waitcnt vmcnt(2)
	v_pk_add_f32 v[40:41], v[40:41], 1.0 op_sel_hi:[1,0]
	s_waitcnt vmcnt(1)
	v_pk_mul_f32 v[44:45], v[50:51], v[44:45]
	v_pk_mul_f32 v[46:47], v[48:49], v[46:47]
	v_pk_fma_f32 v[2:3], v[40:41], v[44:45], v[2:3]
	v_pk_add_f32 v[42:43], v[42:43], 1.0 op_sel_hi:[1,0]
	v_cvt_pk_fp8_f32 v30, v2, v3
	v_pk_fma_f32 v[4:5], v[42:43], v[46:47], v[4:5]
	ds_write_b128 v200, v[2:5] offset:6144
	v_cvt_pk_fp8_f32 v30, v4, v5 op_sel:[0,0,1]
	s_nop 1
	v_mov_b32_e32 v240, v30
	global_load_dwordx4 v[2:5], v209, s[0:1]
	global_load_dwordx4 v[40:43], v209, s[20:21]
	global_load_dwordx4 v[44:47], v[16:17], off
	global_store_dword v[60:61], v240, off offset:1536
	v_pk_mul_f32 v[30:31], v[32:33], v[38:39] op_sel_hi:[1,0]
	s_waitcnt vmcnt(2)
	v_pk_add_f32 v[36:37], v[40:41], 1.0 op_sel_hi:[1,0]
	s_waitcnt vmcnt(1)
	v_pk_mul_f32 v[30:31], v[30:31], v[44:45]
	v_pk_mul_f32 v[32:33], v[34:35], v[46:47]
	v_pk_fma_f32 v[2:3], v[36:37], v[30:31], v[2:3]
	v_mov_b32_e32 v30, 0
	v_cvt_pk_fp8_f32 v30, v2, v3
	v_pk_add_f32 v[34:35], v[42:43], 1.0 op_sel_hi:[1,0]
	s_nop 0
	v_pk_fma_f32 v[4:5], v[34:35], v[32:33], v[4:5]
	ds_write_b128 v200, v[2:5] offset:7168
	v_cvt_pk_fp8_f32 v30, v4, v5 op_sel:[0,0,1]
	global_store_dword v[60:61], v30, off offset:1792
	s_waitcnt lgkmcnt(0)
	s_barrier
	ds_read_b128 v[2:5], v210
	s_waitcnt lgkmcnt(0)
	v_mfma_f32_16x16x4_f32 v[30:33], v2, v1, 0
	v_mfma_f32_16x16x4_f32 v[34:37], v2, v39, 0
	v_mfma_f32_16x16x4_f32 v[30:33], v3, v62, v[30:33]
	v_mfma_f32_16x16x4_f32 v[34:37], v3, v63, v[34:37]
	v_mfma_f32_16x16x4_f32 v[30:33], v4, v64, v[30:33]
	v_mfma_f32_16x16x4_f32 v[34:37], v4, v65, v[34:37]
	v_mfma_f32_16x16x4_f32 v[30:33], v5, v66, v[30:33]
	v_mfma_f32_16x16x4_f32 v[2:5], v5, v67, v[34:37]
	s_nop 7
	ds_read_b128 v[34:37], v210 offset:64
	s_waitcnt lgkmcnt(0)
	v_mfma_f32_16x16x4_f32 v[30:33], v34, v68, v[30:33]
	v_mfma_f32_16x16x4_f32 v[2:5], v34, v69, v[2:5]
	v_mfma_f32_16x16x4_f32 v[30:33], v35, v70, v[30:33]
	v_mfma_f32_16x16x4_f32 v[2:5], v35, v71, v[2:5]
	v_mfma_f32_16x16x4_f32 v[30:33], v36, v72, v[30:33]
	v_mfma_f32_16x16x4_f32 v[2:5], v36, v73, v[2:5]
	v_mfma_f32_16x16x4_f32 v[30:33], v37, v74, v[30:33]
	v_mfma_f32_16x16x4_f32 v[2:5], v37, v75, v[2:5]
	ds_read_b128 v[34:37], v210 offset:128
	s_waitcnt lgkmcnt(0)
	v_mfma_f32_16x16x4_f32 v[30:33], v34, v76, v[30:33]
	v_mfma_f32_16x16x4_f32 v[2:5], v34, v77, v[2:5]
	v_mfma_f32_16x16x4_f32 v[30:33], v35, v78, v[30:33]
	v_mfma_f32_16x16x4_f32 v[2:5], v35, v79, v[2:5]
	v_mfma_f32_16x16x4_f32 v[30:33], v36, v80, v[30:33]
	v_mfma_f32_16x16x4_f32 v[2:5], v36, v81, v[2:5]
	v_mfma_f32_16x16x4_f32 v[30:33], v37, v82, v[30:33]
	v_mfma_f32_16x16x4_f32 v[2:5], v37, v83, v[2:5]
	ds_read_b128 v[34:37], v210 offset:192
	s_waitcnt lgkmcnt(0)
	v_mfma_f32_16x16x4_f32 v[30:33], v34, v84, v[30:33]
	v_mfma_f32_16x16x4_f32 v[2:5], v34, v85, v[2:5]
	v_mfma_f32_16x16x4_f32 v[30:33], v35, v86, v[30:33]
	v_mfma_f32_16x16x4_f32 v[2:5], v35, v87, v[2:5]
	v_mfma_f32_16x16x4_f32 v[30:33], v36, v88, v[30:33]
	v_mfma_f32_16x16x4_f32 v[2:5], v36, v89, v[2:5]
	v_mfma_f32_16x16x4_f32 v[30:33], v37, v90, v[30:33]
	v_mfma_f32_16x16x4_f32 v[2:5], v37, v91, v[2:5]
	ds_read_b128 v[34:37], v210 offset:256
	s_waitcnt lgkmcnt(0)
	v_mfma_f32_16x16x4_f32 v[30:33], v34, v92, v[30:33]
	v_mfma_f32_16x16x4_f32 v[2:5], v34, v93, v[2:5]
	v_mfma_f32_16x16x4_f32 v[30:33], v35, v94, v[30:33]
	v_mfma_f32_16x16x4_f32 v[2:5], v35, v95, v[2:5]
	v_mfma_f32_16x16x4_f32 v[30:33], v36, v96, v[30:33]
	v_mfma_f32_16x16x4_f32 v[2:5], v36, v97, v[2:5]
	v_mfma_f32_16x16x4_f32 v[30:33], v37, v98, v[30:33]
	v_mfma_f32_16x16x4_f32 v[2:5], v37, v99, v[2:5]
	ds_read_b128 v[34:37], v210 offset:320
	s_waitcnt lgkmcnt(0)
	v_mfma_f32_16x16x4_f32 v[30:33], v34, v100, v[30:33]
	v_mfma_f32_16x16x4_f32 v[2:5], v34, v101, v[2:5]
	v_mfma_f32_16x16x4_f32 v[30:33], v35, v102, v[30:33]
	v_mfma_f32_16x16x4_f32 v[2:5], v35, v103, v[2:5]
	v_mfma_f32_16x16x4_f32 v[30:33], v36, v104, v[30:33]
	v_mfma_f32_16x16x4_f32 v[2:5], v36, v105, v[2:5]
	v_mfma_f32_16x16x4_f32 v[30:33], v37, v106, v[30:33]
	v_mfma_f32_16x16x4_f32 v[2:5], v37, v107, v[2:5]
	ds_read_b128 v[34:37], v210 offset:384
	s_waitcnt lgkmcnt(0)
	v_mfma_f32_16x16x4_f32 v[30:33], v34, v108, v[30:33]
	v_mfma_f32_16x16x4_f32 v[2:5], v34, v109, v[2:5]
	v_mfma_f32_16x16x4_f32 v[30:33], v35, v110, v[30:33]
	v_mfma_f32_16x16x4_f32 v[2:5], v35, v111, v[2:5]
	v_mfma_f32_16x16x4_f32 v[30:33], v36, v112, v[30:33]
	v_mfma_f32_16x16x4_f32 v[2:5], v36, v113, v[2:5]
	v_mfma_f32_16x16x4_f32 v[30:33], v37, v114, v[30:33]
	v_mfma_f32_16x16x4_f32 v[2:5], v37, v115, v[2:5]
	ds_read_b128 v[34:37], v210 offset:448
	s_waitcnt lgkmcnt(0)
	v_mfma_f32_16x16x4_f32 v[30:33], v34, v116, v[30:33]
	v_mfma_f32_16x16x4_f32 v[2:5], v34, v117, v[2:5]
	v_mfma_f32_16x16x4_f32 v[30:33], v35, v118, v[30:33]
	v_mfma_f32_16x16x4_f32 v[2:5], v35, v119, v[2:5]
	v_mfma_f32_16x16x4_f32 v[30:33], v36, v120, v[30:33]
	v_mfma_f32_16x16x4_f32 v[2:5], v36, v121, v[2:5]
	v_mfma_f32_16x16x4_f32 v[30:33], v37, v122, v[30:33]
	v_mfma_f32_16x16x4_f32 v[2:5], v37, v123, v[2:5]
	ds_read_b128 v[34:37], v210 offset:512
	s_waitcnt lgkmcnt(0)
	v_mfma_f32_16x16x4_f32 v[30:33], v34, v124, v[30:33]
	v_mfma_f32_16x16x4_f32 v[2:5], v34, v125, v[2:5]
	v_mfma_f32_16x16x4_f32 v[30:33], v35, v126, v[30:33]
	v_mfma_f32_16x16x4_f32 v[2:5], v35, v127, v[2:5]
	v_mfma_f32_16x16x4_f32 v[30:33], v36, v128, v[30:33]
	v_mfma_f32_16x16x4_f32 v[2:5], v36, v129, v[2:5]
	v_mfma_f32_16x16x4_f32 v[30:33], v37, v130, v[30:33]
	v_mfma_f32_16x16x4_f32 v[2:5], v37, v131, v[2:5]
	ds_read_b128 v[34:37], v210 offset:576
	s_waitcnt lgkmcnt(0)
	v_mfma_f32_16x16x4_f32 v[30:33], v34, v132, v[30:33]
	v_mfma_f32_16x16x4_f32 v[2:5], v34, v133, v[2:5]
	v_mfma_f32_16x16x4_f32 v[30:33], v35, v134, v[30:33]
	v_mfma_f32_16x16x4_f32 v[2:5], v35, v135, v[2:5]
	v_mfma_f32_16x16x4_f32 v[30:33], v36, v136, v[30:33]
	v_mfma_f32_16x16x4_f32 v[2:5], v36, v137, v[2:5]
	v_mfma_f32_16x16x4_f32 v[30:33], v37, v138, v[30:33]
	v_mfma_f32_16x16x4_f32 v[2:5], v37, v139, v[2:5]
	ds_read_b128 v[34:37], v210 offset:640
	s_waitcnt lgkmcnt(0)
	v_mfma_f32_16x16x4_f32 v[30:33], v34, v140, v[30:33]
	v_mfma_f32_16x16x4_f32 v[2:5], v34, v141, v[2:5]
	v_mfma_f32_16x16x4_f32 v[30:33], v35, v142, v[30:33]
	v_mfma_f32_16x16x4_f32 v[2:5], v35, v143, v[2:5]
	v_mfma_f32_16x16x4_f32 v[30:33], v36, v144, v[30:33]
	v_mfma_f32_16x16x4_f32 v[2:5], v36, v145, v[2:5]
	v_mfma_f32_16x16x4_f32 v[30:33], v37, v146, v[30:33]
	v_mfma_f32_16x16x4_f32 v[2:5], v37, v147, v[2:5]
	ds_read_b128 v[34:37], v210 offset:704
	s_waitcnt lgkmcnt(0)
	v_mfma_f32_16x16x4_f32 v[30:33], v34, v148, v[30:33]
	v_mfma_f32_16x16x4_f32 v[2:5], v34, v149, v[2:5]
	v_mfma_f32_16x16x4_f32 v[30:33], v35, v150, v[30:33]
	v_mfma_f32_16x16x4_f32 v[2:5], v35, v151, v[2:5]
	v_mfma_f32_16x16x4_f32 v[30:33], v36, v152, v[30:33]
	v_mfma_f32_16x16x4_f32 v[2:5], v36, v153, v[2:5]
	v_mfma_f32_16x16x4_f32 v[30:33], v37, v154, v[30:33]
	v_mfma_f32_16x16x4_f32 v[2:5], v37, v155, v[2:5]
	ds_read_b128 v[34:37], v210 offset:768
	s_waitcnt lgkmcnt(0)
	v_mfma_f32_16x16x4_f32 v[30:33], v34, v156, v[30:33]
	v_mfma_f32_16x16x4_f32 v[2:5], v34, v157, v[2:5]
	v_mfma_f32_16x16x4_f32 v[30:33], v35, v158, v[30:33]
	v_mfma_f32_16x16x4_f32 v[2:5], v35, v159, v[2:5]
	v_mfma_f32_16x16x4_f32 v[30:33], v36, v160, v[30:33]
	v_mfma_f32_16x16x4_f32 v[2:5], v36, v161, v[2:5]
	v_mfma_f32_16x16x4_f32 v[30:33], v37, v162, v[30:33]
	v_mfma_f32_16x16x4_f32 v[2:5], v37, v163, v[2:5]
	ds_read_b128 v[34:37], v210 offset:832
	s_waitcnt lgkmcnt(0)
	v_mfma_f32_16x16x4_f32 v[30:33], v34, v164, v[30:33]
	v_mfma_f32_16x16x4_f32 v[2:5], v34, v165, v[2:5]
	v_mfma_f32_16x16x4_f32 v[30:33], v35, v166, v[30:33]
	v_mfma_f32_16x16x4_f32 v[2:5], v35, v167, v[2:5]
	v_mfma_f32_16x16x4_f32 v[30:33], v36, v168, v[30:33]
	v_mfma_f32_16x16x4_f32 v[2:5], v36, v169, v[2:5]
	v_mfma_f32_16x16x4_f32 v[30:33], v37, v170, v[30:33]
	v_mfma_f32_16x16x4_f32 v[2:5], v37, v171, v[2:5]
	ds_read_b128 v[34:37], v210 offset:896
	s_waitcnt lgkmcnt(0)
	v_mfma_f32_16x16x4_f32 v[30:33], v34, v172, v[30:33]
	v_mfma_f32_16x16x4_f32 v[2:5], v34, v173, v[2:5]
	v_mfma_f32_16x16x4_f32 v[30:33], v35, v174, v[30:33]
	v_mfma_f32_16x16x4_f32 v[2:5], v35, v175, v[2:5]
	v_mfma_f32_16x16x4_f32 v[30:33], v36, v176, v[30:33]
	v_mfma_f32_16x16x4_f32 v[2:5], v36, v177, v[2:5]
	v_mfma_f32_16x16x4_f32 v[30:33], v37, v178, v[30:33]
	v_mfma_f32_16x16x4_f32 v[2:5], v37, v179, v[2:5]
	ds_read_b128 v[34:37], v210 offset:960
	s_waitcnt lgkmcnt(0)
	v_mfma_f32_16x16x4_f32 v[30:33], v34, v180, v[30:33]
	v_mfma_f32_16x16x4_f32 v[2:5], v34, v181, v[2:5]
	v_mfma_f32_16x16x4_f32 v[30:33], v35, v182, v[30:33]
	v_mfma_f32_16x16x4_f32 v[2:5], v35, v183, v[2:5]
	v_mfma_f32_16x16x4_f32 v[30:33], v36, v184, v[30:33]
	v_mfma_f32_16x16x4_f32 v[2:5], v36, v185, v[2:5]
	v_mfma_f32_16x16x4_f32 v[30:33], v37, v186, v[30:33]
	v_mfma_f32_16x16x4_f32 v[2:5], v37, v187, v[2:5]
	s_nop 9
	ds_write2_b32 v211, v30, v2 offset1:16
	ds_write2_b32 v211, v31, v3 offset0:32 offset1:48
	ds_write2_b32 v211, v32, v4 offset0:64 offset1:80
	ds_write2_b32 v211, v33, v5 offset0:96 offset1:112
	s_waitcnt lgkmcnt(0)
	s_barrier
	global_load_dword v4, v[18:19], off
	ds_read2st64_b32 v[2:3], v198 offset1:8
	ds_bpermute_b32 v31, v192, v197
	s_waitcnt vmcnt(0) lgkmcnt(1)
	v_add_f32_e32 v2, v4, v2
	v_add_f32_e32 v4, v2, v3
	ds_read2st64_b32 v[2:3], v198 offset0:16 offset1:24
	s_waitcnt lgkmcnt(0)
	v_add_f32_e32 v2, v4, v2
	v_add_f32_e32 v4, v2, v3
	ds_read2st64_b32 v[2:3], v198 offset0:32 offset1:40
	s_waitcnt lgkmcnt(0)
	v_add_f32_e32 v2, v4, v2
	v_add_f32_e32 v4, v2, v3
	ds_read2st64_b32 v[2:3], v198 offset0:48 offset1:56
	s_waitcnt lgkmcnt(0)
	v_add_f32_e32 v2, v4, v2
	v_add_f32_e32 v3, v2, v3
	ds_bpermute_b32 v5, v192, v3
	s_waitcnt lgkmcnt(0)
	v_cmp_lt_f32_e64 s[20:21], v3, v5
	v_cmp_nlt_f32_e32 vcc, v3, v5
	s_and_saveexec_b64 s[22:23], vcc
	v_cmp_eq_f32_e32 vcc, v3, v5
	v_cmp_lt_i32_e64 s[0:1], v31, v197
	s_and_b64 s[0:1], vcc, s[0:1]
	s_andn2_b64 s[20:21], s[20:21], exec
	s_and_b64 s[0:1], s[0:1], exec
	s_or_b64 s[20:21], s[20:21], s[0:1]
	s_or_b64 exec, exec, s[22:23]
	v_mov_b32_e32 v4, v3
	v_mov_b32_e32 v30, v3
	v_mov_b32_e32 v2, v197
	s_and_saveexec_b64 s[0:1], s[20:21]
	v_mov_b32_e32 v4, v5
	v_mov_b32_e32 v30, v5
	v_mov_b32_e32 v2, v31
	s_or_b64 exec, exec, s[0:1]
	s_nop 1
	v_mov_b32_dpp v5, v4 row_ror:8 row_mask:0xf bank_mask:0xf
	s_nop 1
	v_mov_b32_dpp v31, v2 row_ror:8 row_mask:0xf bank_mask:0xf
	s_waitcnt lgkmcnt(1)
	v_cmp_lt_f32_e64 s[20:21], v30, v5
	v_cmp_nlt_f32_e32 vcc, v30, v5
	s_and_saveexec_b64 s[22:23], vcc
	s_cbranch_execz .LBB0_688
	v_cmp_eq_f32_e32 vcc, v30, v5
	s_waitcnt lgkmcnt(0)
	v_cmp_lt_i32_e64 s[0:1], v31, v2
	s_and_b64 s[0:1], vcc, s[0:1]
	s_andn2_b64 s[20:21], s[20:21], exec
	s_and_b64 s[0:1], s[0:1], exec
	s_or_b64 s[20:21], s[20:21], s[0:1]

.LBB0_690:
	s_or_b64 exec, exec, s[0:1]
	s_nop 1
	v_mov_b32_dpp v5, v4 row_ror:4 row_mask:0xf bank_mask:0xf
	s_waitcnt lgkmcnt(1)
	s_nop 1
	v_mov_b32_dpp v31, v2 row_ror:4 row_mask:0xf bank_mask:0xf
	s_waitcnt lgkmcnt(1)
	v_cmp_lt_f32_e64 s[20:21], v30, v5
	v_cmp_nlt_f32_e32 vcc, v30, v5
	s_and_saveexec_b64 s[22:23], vcc
	s_cbranch_execz .LBB0_692
	v_cmp_eq_f32_e32 vcc, v30, v5
	s_waitcnt lgkmcnt(0)
	v_cmp_lt_i32_e64 s[0:1], v31, v2
	s_and_b64 s[0:1], vcc, s[0:1]
	s_andn2_b64 s[20:21], s[20:21], exec
	s_and_b64 s[0:1], s[0:1], exec
	s_or_b64 s[20:21], s[20:21], s[0:1]

.LBB0_694:
	s_or_b64 exec, exec, s[0:1]
	s_nop 1
	v_mov_b32_dpp v5, v4 quad_perm:[2,3,0,1] row_mask:0xf bank_mask:0xf
	s_waitcnt lgkmcnt(1)
	s_nop 1
	v_mov_b32_dpp v31, v2 quad_perm:[2,3,0,1] row_mask:0xf bank_mask:0xf
	s_waitcnt lgkmcnt(1)
	v_cmp_lt_f32_e64 s[20:21], v30, v5
	v_cmp_nlt_f32_e32 vcc, v30, v5
	s_and_saveexec_b64 s[22:23], vcc
	s_cbranch_execz .LBB0_696
	v_cmp_eq_f32_e32 vcc, v30, v5
	s_waitcnt lgkmcnt(0)
	v_cmp_lt_i32_e64 s[0:1], v31, v2
	s_and_b64 s[0:1], vcc, s[0:1]
	s_andn2_b64 s[20:21], s[20:21], exec
	s_and_b64 s[0:1], s[0:1], exec
	s_or_b64 s[20:21], s[20:21], s[0:1]

.LBB0_698:
	s_or_b64 exec, exec, s[0:1]
	s_nop 1
	v_mov_b32_dpp v4, v4 quad_perm:[1,0,3,2] row_mask:0xf bank_mask:0xf
	s_nop 1
	v_mov_b32_dpp v5, v2 quad_perm:[1,0,3,2] row_mask:0xf bank_mask:0xf
	s_waitcnt lgkmcnt(1)
	v_cmp_lt_f32_e64 s[20:21], v30, v4
	v_cmp_nlt_f32_e32 vcc, v30, v4
	s_and_saveexec_b64 s[22:23], vcc
	s_cbranch_execz .LBB0_700
	v_cmp_eq_f32_e32 vcc, v30, v4
	s_waitcnt lgkmcnt(0)
	v_cmp_lt_i32_e64 s[0:1], v5, v2
	s_and_b64 s[0:1], vcc, s[0:1]
	s_andn2_b64 s[20:21], s[20:21], exec
	s_and_b64 s[0:1], s[0:1], exec
	s_or_b64 s[20:21], s[20:21], s[0:1]

.LBB0_702:
	s_or_b64 exec, exec, s[0:1]
	v_cmp_ne_u32_e32 vcc, v197, v2
	ds_bpermute_b32 v33, v192, v197
	s_nop 0
	v_cndmask_b32_e32 v4, v213, v3, vcc
	ds_bpermute_b32 v32, v192, v4
	s_waitcnt lgkmcnt(0)
	v_cmp_lt_f32_e64 s[20:21], v4, v32
	v_cmp_nlt_f32_e32 vcc, v4, v32
	s_and_saveexec_b64 s[22:23], vcc
	v_cmp_eq_f32_e32 vcc, v4, v32
	v_cmp_lt_i32_e64 s[0:1], v33, v197
	s_and_b64 s[0:1], vcc, s[0:1]
	s_andn2_b64 s[20:21], s[20:21], exec
	s_and_b64 s[0:1], s[0:1], exec
	s_or_b64 s[20:21], s[20:21], s[0:1]
	s_or_b64 exec, exec, s[22:23]
	v_mov_b32_e32 v5, v4
	v_mov_b32_e32 v31, v4
	v_mov_b32_e32 v3, v197
	s_and_saveexec_b64 s[0:1], s[20:21]
	v_mov_b32_e32 v5, v32
	v_mov_b32_e32 v31, v32
	v_mov_b32_e32 v3, v33
	s_or_b64 exec, exec, s[0:1]
	s_nop 1
	v_mov_b32_dpp v32, v5 row_ror:8 row_mask:0xf bank_mask:0xf
	s_nop 1
	v_mov_b32_dpp v33, v3 row_ror:8 row_mask:0xf bank_mask:0xf
	s_waitcnt lgkmcnt(1)
	v_cmp_lt_f32_e64 s[20:21], v31, v32
	v_cmp_nlt_f32_e32 vcc, v31, v32
	s_and_saveexec_b64 s[22:23], vcc
	s_cbranch_execz .LBB0_708
	v_cmp_eq_f32_e32 vcc, v31, v32
	s_waitcnt lgkmcnt(0)
	v_cmp_lt_i32_e64 s[0:1], v33, v3
	s_and_b64 s[0:1], vcc, s[0:1]
	s_andn2_b64 s[20:21], s[20:21], exec
	s_and_b64 s[0:1], s[0:1], exec
	s_or_b64 s[20:21], s[20:21], s[0:1]

.LBB0_710:
	s_or_b64 exec, exec, s[0:1]
	s_nop 1
	v_mov_b32_dpp v32, v5 row_ror:4 row_mask:0xf bank_mask:0xf
	s_waitcnt lgkmcnt(1)
	s_nop 1
	v_mov_b32_dpp v33, v3 row_ror:4 row_mask:0xf bank_mask:0xf
	s_waitcnt lgkmcnt(1)
	v_cmp_lt_f32_e64 s[20:21], v31, v32
	v_cmp_nlt_f32_e32 vcc, v31, v32
	s_and_saveexec_b64 s[22:23], vcc
	s_cbranch_execz .LBB0_712
	v_cmp_eq_f32_e32 vcc, v31, v32
	s_waitcnt lgkmcnt(0)
	v_cmp_lt_i32_e64 s[0:1], v33, v3
	s_and_b64 s[0:1], vcc, s[0:1]
	s_andn2_b64 s[20:21], s[20:21], exec
	s_and_b64 s[0:1], s[0:1], exec
	s_or_b64 s[20:21], s[20:21], s[0:1]

.LBB0_714:
	s_or_b64 exec, exec, s[0:1]
	s_nop 1
	v_mov_b32_dpp v32, v5 quad_perm:[2,3,0,1] row_mask:0xf bank_mask:0xf
	s_waitcnt lgkmcnt(1)
	s_nop 1
	v_mov_b32_dpp v33, v3 quad_perm:[2,3,0,1] row_mask:0xf bank_mask:0xf
	s_waitcnt lgkmcnt(1)
	v_cmp_lt_f32_e64 s[20:21], v31, v32
	v_cmp_nlt_f32_e32 vcc, v31, v32
	s_and_saveexec_b64 s[22:23], vcc
	s_cbranch_execz .LBB0_716
	v_cmp_eq_f32_e32 vcc, v31, v32
	s_waitcnt lgkmcnt(0)
	v_cmp_lt_i32_e64 s[0:1], v33, v3
	s_and_b64 s[0:1], vcc, s[0:1]
	s_andn2_b64 s[20:21], s[20:21], exec
	s_and_b64 s[0:1], s[0:1], exec
	s_or_b64 s[20:21], s[20:21], s[0:1]

.LBB0_718:
	s_or_b64 exec, exec, s[0:1]
	s_nop 1
	v_mov_b32_dpp v5, v5 quad_perm:[1,0,3,2] row_mask:0xf bank_mask:0xf
	s_nop 1
	v_mov_b32_dpp v32, v3 quad_perm:[1,0,3,2] row_mask:0xf bank_mask:0xf
	s_waitcnt lgkmcnt(1)
	v_cmp_lt_f32_e64 s[20:21], v31, v5
	v_cmp_nlt_f32_e32 vcc, v31, v5
	s_and_saveexec_b64 s[22:23], vcc
	s_cbranch_execz .LBB0_720
	v_cmp_eq_f32_e32 vcc, v31, v5
	s_waitcnt lgkmcnt(0)
	v_cmp_lt_i32_e64 s[0:1], v32, v3
	s_and_b64 s[0:1], vcc, s[0:1]
	s_andn2_b64 s[20:21], s[20:21], exec
	s_and_b64 s[0:1], s[0:1], exec
	s_or_b64 s[20:21], s[20:21], s[0:1]

.LBB0_722:
	s_or_b64 exec, exec, s[0:1]
	v_cmp_ne_u32_e32 vcc, v197, v3
	ds_bpermute_b32 v35, v192, v197
	s_nop 0
	v_cndmask_b32_e32 v5, v213, v4, vcc
	ds_bpermute_b32 v34, v192, v5
	s_waitcnt lgkmcnt(0)
	v_cmp_lt_f32_e64 s[20:21], v5, v34
	v_cmp_nlt_f32_e32 vcc, v5, v34
	s_and_saveexec_b64 s[22:23], vcc
	v_cmp_eq_f32_e32 vcc, v5, v34
	v_cmp_lt_i32_e64 s[0:1], v35, v197
	s_and_b64 s[0:1], vcc, s[0:1]
	s_andn2_b64 s[20:21], s[20:21], exec
	s_and_b64 s[0:1], s[0:1], exec
	s_or_b64 s[20:21], s[20:21], s[0:1]
	s_or_b64 exec, exec, s[22:23]
	v_mov_b32_e32 v33, v5
	v_mov_b32_e32 v32, v5
	v_mov_b32_e32 v4, v197
	s_and_saveexec_b64 s[0:1], s[20:21]
	v_mov_b32_e32 v33, v34
	v_mov_b32_e32 v32, v34
	v_mov_b32_e32 v4, v35
	s_or_b64 exec, exec, s[0:1]
	s_nop 1
	v_mov_b32_dpp v34, v33 row_ror:8 row_mask:0xf bank_mask:0xf
	s_nop 1
	v_mov_b32_dpp v35, v4 row_ror:8 row_mask:0xf bank_mask:0xf
	s_waitcnt lgkmcnt(1)
	v_cmp_lt_f32_e64 s[20:21], v32, v34
	v_cmp_nlt_f32_e32 vcc, v32, v34
	s_and_saveexec_b64 s[22:23], vcc
	s_cbranch_execz .LBB0_728
	v_cmp_eq_f32_e32 vcc, v32, v34
	s_waitcnt lgkmcnt(0)
	v_cmp_lt_i32_e64 s[0:1], v35, v4
	s_and_b64 s[0:1], vcc, s[0:1]
	s_andn2_b64 s[20:21], s[20:21], exec
	s_and_b64 s[0:1], s[0:1], exec
	s_or_b64 s[20:21], s[20:21], s[0:1]

.LBB0_730:
	s_or_b64 exec, exec, s[0:1]
	s_nop 1
	v_mov_b32_dpp v34, v33 row_ror:4 row_mask:0xf bank_mask:0xf
	s_waitcnt lgkmcnt(1)
	s_nop 1
	v_mov_b32_dpp v35, v4 row_ror:4 row_mask:0xf bank_mask:0xf
	s_waitcnt lgkmcnt(1)
	v_cmp_lt_f32_e64 s[20:21], v32, v34
	v_cmp_nlt_f32_e32 vcc, v32, v34
	s_and_saveexec_b64 s[22:23], vcc
	s_cbranch_execz .LBB0_732
	v_cmp_eq_f32_e32 vcc, v32, v34
	s_waitcnt lgkmcnt(0)
	v_cmp_lt_i32_e64 s[0:1], v35, v4
	s_and_b64 s[0:1], vcc, s[0:1]
	s_andn2_b64 s[20:21], s[20:21], exec
	s_and_b64 s[0:1], s[0:1], exec
	s_or_b64 s[20:21], s[20:21], s[0:1]

.LBB0_734:
	s_or_b64 exec, exec, s[0:1]
	s_nop 1
	v_mov_b32_dpp v34, v33 quad_perm:[2,3,0,1] row_mask:0xf bank_mask:0xf
	s_waitcnt lgkmcnt(1)
	s_nop 1
	v_mov_b32_dpp v35, v4 quad_perm:[2,3,0,1] row_mask:0xf bank_mask:0xf
	s_waitcnt lgkmcnt(1)
	v_cmp_lt_f32_e64 s[20:21], v32, v34
	v_cmp_nlt_f32_e32 vcc, v32, v34
	s_and_saveexec_b64 s[22:23], vcc
	s_cbranch_execz .LBB0_736
	v_cmp_eq_f32_e32 vcc, v32, v34
	s_waitcnt lgkmcnt(0)
	v_cmp_lt_i32_e64 s[0:1], v35, v4
	s_and_b64 s[0:1], vcc, s[0:1]
	s_andn2_b64 s[20:21], s[20:21], exec
	s_and_b64 s[0:1], s[0:1], exec
	s_or_b64 s[20:21], s[20:21], s[0:1]

.LBB0_738:
	s_or_b64 exec, exec, s[0:1]
	s_nop 1
	v_mov_b32_dpp v33, v33 quad_perm:[1,0,3,2] row_mask:0xf bank_mask:0xf
	s_nop 1
	v_mov_b32_dpp v34, v4 quad_perm:[1,0,3,2] row_mask:0xf bank_mask:0xf
	s_waitcnt lgkmcnt(1)
	v_cmp_lt_f32_e64 s[20:21], v32, v33
	v_cmp_nlt_f32_e32 vcc, v32, v33
	s_and_saveexec_b64 s[22:23], vcc
	s_cbranch_execz .LBB0_740
	v_cmp_eq_f32_e32 vcc, v32, v33
	s_waitcnt lgkmcnt(0)
	v_cmp_lt_i32_e64 s[0:1], v34, v4
	s_and_b64 s[0:1], vcc, s[0:1]
	s_andn2_b64 s[20:21], s[20:21], exec
	s_and_b64 s[0:1], s[0:1], exec
	s_or_b64 s[20:21], s[20:21], s[0:1]

.LBB0_742:
	s_or_b64 exec, exec, s[0:1]
	v_cmp_ne_u32_e32 vcc, v197, v4
	s_waitcnt lgkmcnt(0)
	ds_bpermute_b32 v34, v192, v197
	v_cndmask_b32_e32 v33, v213, v5, vcc
	ds_bpermute_b32 v35, v192, v33
	s_waitcnt lgkmcnt(0)
	v_cmp_lt_f32_e64 s[20:21], v33, v35
	v_cmp_nlt_f32_e32 vcc, v33, v35
	s_and_saveexec_b64 s[22:23], vcc
	v_cmp_eq_f32_e32 vcc, v33, v35
	v_cmp_lt_i32_e64 s[0:1], v34, v197
	s_and_b64 s[0:1], vcc, s[0:1]
	s_andn2_b64 s[20:21], s[20:21], exec
	s_and_b64 s[0:1], s[0:1], exec
	s_or_b64 s[20:21], s[20:21], s[0:1]
	s_or_b64 exec, exec, s[22:23]
	v_mov_b32_e32 v5, v197
	s_and_saveexec_b64 s[0:1], s[20:21]
	v_mov_b32_e32 v33, v35
	v_mov_b32_e32 v5, v34
	s_or_b64 exec, exec, s[0:1]
	s_nop 1
	v_mov_b32_dpp v35, v33 row_ror:8 row_mask:0xf bank_mask:0xf
	s_nop 1
	v_mov_b32_dpp v34, v5 row_ror:8 row_mask:0xf bank_mask:0xf
	s_waitcnt lgkmcnt(1)
	v_cmp_lt_f32_e64 s[20:21], v33, v35
	v_cmp_nlt_f32_e32 vcc, v33, v35
	s_and_saveexec_b64 s[22:23], vcc
	s_cbranch_execz .LBB0_748
	v_cmp_eq_f32_e32 vcc, v33, v35
	s_waitcnt lgkmcnt(0)
	v_cmp_lt_i32_e64 s[0:1], v34, v5
	s_and_b64 s[0:1], vcc, s[0:1]
	s_andn2_b64 s[20:21], s[20:21], exec
	s_and_b64 s[0:1], s[0:1], exec
	s_or_b64 s[20:21], s[20:21], s[0:1]

.LBB0_750:
	s_or_b64 exec, exec, s[0:1]
	s_nop 1
	v_mov_b32_dpp v35, v33 row_ror:4 row_mask:0xf bank_mask:0xf
	s_waitcnt lgkmcnt(1)
	s_nop 1
	v_mov_b32_dpp v34, v5 row_ror:4 row_mask:0xf bank_mask:0xf
	s_waitcnt lgkmcnt(1)
	v_cmp_lt_f32_e64 s[20:21], v33, v35
	v_cmp_nlt_f32_e32 vcc, v33, v35
	s_and_saveexec_b64 s[22:23], vcc
	s_cbranch_execz .LBB0_752
	v_cmp_eq_f32_e32 vcc, v33, v35
	s_waitcnt lgkmcnt(0)
	v_cmp_lt_i32_e64 s[0:1], v34, v5
	s_and_b64 s[0:1], vcc, s[0:1]
	s_andn2_b64 s[20:21], s[20:21], exec
	s_and_b64 s[0:1], s[0:1], exec
	s_or_b64 s[20:21], s[20:21], s[0:1]

.LBB0_754:
	s_or_b64 exec, exec, s[0:1]
	s_nop 1
	v_mov_b32_dpp v35, v33 quad_perm:[2,3,0,1] row_mask:0xf bank_mask:0xf
	s_waitcnt lgkmcnt(1)
	s_nop 1
	v_mov_b32_dpp v34, v5 quad_perm:[2,3,0,1] row_mask:0xf bank_mask:0xf
	s_waitcnt lgkmcnt(1)
	v_cmp_lt_f32_e64 s[20:21], v33, v35
	v_cmp_nlt_f32_e32 vcc, v33, v35
	s_and_saveexec_b64 s[22:23], vcc
	s_cbranch_execz .LBB0_756
	v_cmp_eq_f32_e32 vcc, v33, v35
	s_waitcnt lgkmcnt(0)
	v_cmp_lt_i32_e64 s[0:1], v34, v5
	s_and_b64 s[0:1], vcc, s[0:1]
	s_andn2_b64 s[20:21], s[20:21], exec
	s_and_b64 s[0:1], s[0:1], exec
	s_or_b64 s[20:21], s[20:21], s[0:1]

.LBB0_758:
	s_or_b64 exec, exec, s[0:1]
	s_waitcnt lgkmcnt(0)
	s_nop 1
	v_mov_b32_dpp v34, v33 quad_perm:[1,0,3,2] row_mask:0xf bank_mask:0xf
	s_nop 1
	v_mov_b32_dpp v35, v5 quad_perm:[1,0,3,2] row_mask:0xf bank_mask:0xf
	s_waitcnt lgkmcnt(1)
	v_cmp_lt_f32_e64 s[20:21], v33, v34
	v_cmp_nlt_f32_e32 vcc, v33, v34
	s_and_saveexec_b64 s[22:23], vcc
	s_cbranch_execnz .LBB0_761
	s_or_b64 exec, exec, s[22:23]
	s_and_saveexec_b64 s[0:1], s[20:21]
	s_cbranch_execnz .LBB0_762
